# Plucker write-side chunk sums: two fold levels (permlane32_swap, permlane16_swap) + 4 row_shr steps on 5 regs; totals stored from lanes 15/31/47/63
# speedup vs baseline: 1.0031x; 1.0031x over previous
.LBB1_21:
	s_andn2_b64 vcc, exec, s[26:27]
	s_cbranch_vccnz .LBB1_25
	v_mov_b32_e32 v5, 0
	v_lshlrev_b64 v[2:3], 10, v[4:5]
	v_or_b32_e32 v2, v2, v30
	v_xor_b32_e32 v9, 0x80000000, v16
	v_lshlrev_b64 v[6:7], 5, v[2:3]
	v_lshl_add_u64 v[14:15], s[18:19], 0, v[6:7]
	v_cvt_pk_f16_f32 v6, v17, v9
	v_cvt_f32_f16_e32 v22, v6
	v_cvt_f32_f16_sdwa v23, v6 dst_sel:DWORD dst_unused:UNUSED_PAD src0_sel:WORD_1
	v_mov_b32_e32 v8, v17
	v_xor_b32_e32 v18, 0x80000000, v13
	global_store_dwordx4 v[14:15], v[8:11], off
	v_mov_b32_e32 v19, v12
	v_mov_b32_e32 v20, v5
	v_mov_b32_e32 v21, v5
	v_pk_add_f32 v[8:9], v[8:9], v[22:23] neg_lo:[0,1] neg_hi:[0,1]
	v_cvt_pk_f16_f32 v7, v10, v11
	s_mov_b32 s26, 0x44800000
	global_store_dwordx4 v[14:15], v[18:21], off offset:16
	v_cvt_f32_f16_e32 v14, v7
	v_cvt_f32_f16_sdwa v15, v7 dst_sel:DWORD dst_unused:UNUSED_PAD src0_sel:WORD_1
	v_pk_mul_f32 v[8:9], v[8:9], s[26:27] op_sel_hi:[1,0]
	v_lshlrev_b64 v[2:3], 6, v[2:3]
	v_cvt_pk_f16_f32 v9, v8, v9
	v_cvt_pk_f16_f32 v8, v18, v12
	v_cvt_f32_f16_e32 v22, v8
	v_cvt_f32_f16_sdwa v23, v8 dst_sel:DWORD dst_unused:UNUSED_PAD src0_sel:WORD_1
	v_pk_add_f32 v[14:15], v[10:11], v[14:15] neg_lo:[0,1] neg_hi:[0,1]
	v_lshl_add_u64 v[2:3], s[16:17], 0, v[2:3]
	v_pk_mul_f32 v[14:15], v[14:15], s[26:27] op_sel_hi:[1,0]
	v_mov_b32_e32 v34, v8
	v_cvt_pk_f16_f32 v20, v14, v15
	v_pk_add_f32 v[14:15], v[18:19], v[22:23] neg_lo:[0,1] neg_hi:[0,1]
	v_mov_b32_e32 v22, v6
	v_pk_mul_f32 v[14:15], v[14:15], s[26:27] op_sel_hi:[1,0]
	v_mov_b32_e32 v23, v7
	v_cvt_pk_f16_f32 v21, v14, v15
	v_mov_b32_e32 v35, v5
	v_mov_b32_e32 v36, v5
	v_mov_b32_e32 v37, v5
	global_store_dwordx4 v[2:3], v[6:9], off
	global_store_dwordx4 v[2:3], v[20:23], off offset:16
	global_store_dwordx4 v[2:3], v[34:37], off offset:32
	v_mov_b32_e32 v6, v5
	v_mov_b32_e32 v7, v5
	v_mov_b32_e32 v8, v5
	v_mov_b32_e32 v9, v5
	global_store_dwordx4 v[2:3], v[6:9], off offset:48
	v_mul_f32_e64 v23, v17, -v16
	v_mul_f32_e32 v24, v17, v10
	v_pk_mul_f32 v[8:9], v[16:17], v[16:17]
	v_mul_f32_e32 v25, v17, v11
	v_mul_f32_e64 v6, v17, -v13
	v_mul_f32_e32 v7, v17, v12
	v_mul_f32_e64 v17, v10, -v16
	v_mul_f32_e64 v18, v11, -v16
	v_mul_f32_e32 v19, v16, v13
	v_mul_f32_e64 v20, v12, -v16
	v_pk_mul_f32 v[28:29], v[10:11], v[10:11]
	v_mul_f32_e32 v14, v10, v11
	v_mul_f32_e64 v15, v10, -v13
	v_mul_f32_e32 v16, v10, v12
	v_mul_f32_e64 v10, v11, -v13
	v_mul_f32_e32 v11, v11, v12
	v_pk_mul_f32 v[2:3], v[12:13], v[12:13]
	v_mul_f32_e64 v13, v12, -v13
	v_mov_b32_e32 v36, 0
	s_nop 1
	v_permlane32_swap_b32_e32 v9, v23
	v_permlane32_swap_b32_e32 v24, v25
	v_permlane32_swap_b32_e32 v6, v7
	v_permlane32_swap_b32_e32 v8, v17
	v_permlane32_swap_b32_e32 v18, v19
	v_permlane32_swap_b32_e32 v20, v28
	v_permlane32_swap_b32_e32 v14, v15
	v_permlane32_swap_b32_e32 v16, v29
	v_permlane32_swap_b32_e32 v10, v11
	v_permlane32_swap_b32_e32 v3, v13
	v_permlane32_swap_b32_e32 v2, v36
	v_add_f32_e32 v9, v9, v23
	v_add_f32_e32 v24, v24, v25
	v_add_f32_e32 v6, v6, v7
	v_add_f32_e32 v8, v8, v17
	v_add_f32_e32 v18, v18, v19
	v_add_f32_e32 v20, v20, v28
	v_add_f32_e32 v14, v14, v15
	v_add_f32_e32 v16, v16, v29
	v_add_f32_e32 v10, v10, v11
	v_add_f32_e32 v3, v3, v13
	v_add_f32_e32 v2, v2, v36
	s_nop 0
	v_permlane16_swap_b32_e32 v9, v24
	v_permlane16_swap_b32_e32 v6, v8
	v_permlane16_swap_b32_e32 v18, v20
	v_permlane16_swap_b32_e32 v14, v16
	v_permlane16_swap_b32_e32 v10, v3
	v_add_f32_e32 v9, v9, v24
	v_add_f32_e32 v6, v6, v8
	v_add_f32_e32 v18, v18, v20
	v_add_f32_e32 v14, v14, v16
	v_add_f32_e32 v10, v10, v3
	v_add_f32_dpp v9, v9, v9 row_shr:1 row_mask:0xf bank_mask:0xf bound_ctrl:1
	v_add_f32_dpp v6, v6, v6 row_shr:1 row_mask:0xf bank_mask:0xf bound_ctrl:1
	v_add_f32_dpp v18, v18, v18 row_shr:1 row_mask:0xf bank_mask:0xf bound_ctrl:1
	v_add_f32_dpp v14, v14, v14 row_shr:1 row_mask:0xf bank_mask:0xf bound_ctrl:1
	v_add_f32_dpp v10, v10, v10 row_shr:1 row_mask:0xf bank_mask:0xf bound_ctrl:1
	v_add_f32_dpp v2, v2, v2 row_shr:1 row_mask:0xf bank_mask:0xf bound_ctrl:1
	v_add_f32_dpp v9, v9, v9 row_shr:2 row_mask:0xf bank_mask:0xf bound_ctrl:1
	v_add_f32_dpp v6, v6, v6 row_shr:2 row_mask:0xf bank_mask:0xf bound_ctrl:1
	v_add_f32_dpp v18, v18, v18 row_shr:2 row_mask:0xf bank_mask:0xf bound_ctrl:1
	v_add_f32_dpp v14, v14, v14 row_shr:2 row_mask:0xf bank_mask:0xf bound_ctrl:1
	v_add_f32_dpp v10, v10, v10 row_shr:2 row_mask:0xf bank_mask:0xf bound_ctrl:1
	v_add_f32_dpp v2, v2, v2 row_shr:2 row_mask:0xf bank_mask:0xf bound_ctrl:1
	v_add_f32_dpp v9, v9, v9 row_shr:4 row_mask:0xf bank_mask:0xf bound_ctrl:1
	v_add_f32_dpp v6, v6, v6 row_shr:4 row_mask:0xf bank_mask:0xf bound_ctrl:1
	v_add_f32_dpp v18, v18, v18 row_shr:4 row_mask:0xf bank_mask:0xf bound_ctrl:1
	v_add_f32_dpp v14, v14, v14 row_shr:4 row_mask:0xf bank_mask:0xf bound_ctrl:1
	v_add_f32_dpp v10, v10, v10 row_shr:4 row_mask:0xf bank_mask:0xf bound_ctrl:1
	v_add_f32_dpp v2, v2, v2 row_shr:4 row_mask:0xf bank_mask:0xf bound_ctrl:1
	v_add_f32_dpp v9, v9, v9 row_shr:8 row_mask:0xf bank_mask:0xf bound_ctrl:1
	v_add_f32_dpp v6, v6, v6 row_shr:8 row_mask:0xf bank_mask:0xf bound_ctrl:1
	v_add_f32_dpp v18, v18, v18 row_shr:8 row_mask:0xf bank_mask:0xf bound_ctrl:1
	v_add_f32_dpp v14, v14, v14 row_shr:8 row_mask:0xf bank_mask:0xf bound_ctrl:1
	v_add_f32_dpp v10, v10, v10 row_shr:8 row_mask:0xf bank_mask:0xf bound_ctrl:1
	v_add_f32_dpp v2, v2, v2 row_shr:8 row_mask:0xf bank_mask:0xf bound_ctrl:1
	s_nop 1
	v_add_f32_dpp v2, v2, v2 row_bcast:15 row_mask:0xa bank_mask:0xf
	v_and_b32_e32 v37, 15, v46
	v_cmp_eq_u32_e64 s[52:53], 15, v37
	s_and_saveexec_b64 s[26:27], s[52:53]
	s_cbranch_execz .LBB1_24
	v_lshl_or_b32 v4, v4, 4, s28
	s_movk_i32 s30, 0x60
	v_mov_b64_e32 v[34:35], s[22:23]
	v_mad_u64_u32 v[34:35], s[30:31], v4, s30, v[34:35]
	v_lshrrev_b32_e32 v50, 4, v46
	v_lshlrev_b32_e32 v52, 1, v50
	v_bfe_u32 v51, v50, 1, 1
	v_and_b32_e32 v52, 2, v52
	v_or_b32_e32 v52, v52, v51
	v_cmp_gt_u32_e32 vcc, 2, v50
	v_xor_b32_e32 v51, 1, v50
	v_mov_b32_e32 v55, 0
	v_lshlrev_b32_e32 v54, 2, v52
	v_cndmask_b32_e32 v51, v50, v51, vcc
	v_lshl_add_u64 v[56:57], v[34:35], 0, v[54:55]
	v_lshlrev_b32_e32 v54, 2, v51
	v_lshl_add_u64 v[58:59], v[34:35], 0, v[54:55]
	global_store_dword v[56:57], v9, off
	global_store_dword v[56:57], v6, off offset:16
	global_store_dword v[56:57], v18, off offset:32
	global_store_dword v[56:57], v14, off offset:48
	global_store_dword v[56:57], v10, off offset:64
	global_store_dword v[58:59], v2, off offset:80

.LBB1_27:
	s_andn2_b64 vcc, exec, s[6:7]
	s_cbranch_vccnz .LBB1_31
	v_mov_b32_e32 v5, 0
	v_lshlrev_b64 v[2:3], 10, v[4:5]
	v_or_b32_e32 v2, v2, v30
	v_xor_b32_e32 v9, 0x80000000, v16
	v_lshlrev_b64 v[6:7], 5, v[2:3]
	v_lshl_add_u64 v[14:15], s[18:19], 0, v[6:7]
	v_cvt_pk_f16_f32 v6, v17, v9
	v_cvt_f32_f16_e32 v22, v6
	v_cvt_f32_f16_sdwa v23, v6 dst_sel:DWORD dst_unused:UNUSED_PAD src0_sel:WORD_1
	v_mov_b32_e32 v8, v17
	v_xor_b32_e32 v18, 0x80000000, v13
	global_store_dwordx4 v[14:15], v[8:11], off
	v_mov_b32_e32 v19, v12
	v_mov_b32_e32 v20, v5
	v_mov_b32_e32 v21, v5
	v_pk_add_f32 v[8:9], v[8:9], v[22:23] neg_lo:[0,1] neg_hi:[0,1]
	v_cvt_pk_f16_f32 v7, v10, v11
	s_mov_b32 s6, 0x44800000
	global_store_dwordx4 v[14:15], v[18:21], off offset:16
	v_cvt_f32_f16_e32 v14, v7
	v_cvt_f32_f16_sdwa v15, v7 dst_sel:DWORD dst_unused:UNUSED_PAD src0_sel:WORD_1
	v_pk_mul_f32 v[8:9], v[8:9], s[6:7] op_sel_hi:[1,0]
	v_lshlrev_b64 v[2:3], 6, v[2:3]
	v_cvt_pk_f16_f32 v9, v8, v9
	v_cvt_pk_f16_f32 v8, v18, v12
	v_cvt_f32_f16_e32 v22, v8
	v_cvt_f32_f16_sdwa v23, v8 dst_sel:DWORD dst_unused:UNUSED_PAD src0_sel:WORD_1
	v_pk_add_f32 v[14:15], v[10:11], v[14:15] neg_lo:[0,1] neg_hi:[0,1]
	v_lshl_add_u64 v[2:3], s[16:17], 0, v[2:3]
	v_pk_mul_f32 v[14:15], v[14:15], s[6:7] op_sel_hi:[1,0]
	v_mov_b32_e32 v24, v8
	v_cvt_pk_f16_f32 v20, v14, v15
	v_pk_add_f32 v[14:15], v[18:19], v[22:23] neg_lo:[0,1] neg_hi:[0,1]
	v_mov_b32_e32 v22, v6
	v_pk_mul_f32 v[14:15], v[14:15], s[6:7] op_sel_hi:[1,0]
	v_mov_b32_e32 v23, v7
	v_cvt_pk_f16_f32 v21, v14, v15
	v_mov_b32_e32 v25, v5
	v_mov_b32_e32 v26, v5
	v_mov_b32_e32 v27, v5
	global_store_dwordx4 v[2:3], v[6:9], off
	global_store_dwordx4 v[2:3], v[20:23], off offset:16
	global_store_dwordx4 v[2:3], v[24:27], off offset:32
	v_mov_b32_e32 v6, v5
	v_mov_b32_e32 v7, v5
	v_mov_b32_e32 v8, v5
	v_mov_b32_e32 v9, v5
	global_store_dwordx4 v[2:3], v[6:9], off offset:48
	v_mul_f32_e64 v23, v17, -v16
	v_mul_f32_e32 v24, v17, v10
	v_pk_mul_f32 v[8:9], v[16:17], v[16:17]
	v_mul_f32_e32 v25, v17, v11
	v_mul_f32_e64 v6, v17, -v13
	v_mul_f32_e32 v7, v17, v12
	v_mul_f32_e64 v17, v10, -v16
	v_mul_f32_e64 v18, v11, -v16
	v_mul_f32_e32 v19, v16, v13
	v_mul_f32_e64 v20, v12, -v16
	v_pk_mul_f32 v[26:27], v[10:11], v[10:11]
	v_mul_f32_e32 v14, v10, v11
	v_mul_f32_e64 v15, v10, -v13
	v_mul_f32_e32 v16, v10, v12
	v_mul_f32_e64 v10, v11, -v13
	v_mul_f32_e32 v11, v11, v12
	v_pk_mul_f32 v[2:3], v[12:13], v[12:13]
	v_mul_f32_e64 v13, v12, -v13
	v_mov_b32_e32 v36, 0
	s_nop 1
	v_permlane32_swap_b32_e32 v9, v23
	v_permlane32_swap_b32_e32 v24, v25
	v_permlane32_swap_b32_e32 v6, v7
	v_permlane32_swap_b32_e32 v8, v17
	v_permlane32_swap_b32_e32 v18, v19
	v_permlane32_swap_b32_e32 v20, v26
	v_permlane32_swap_b32_e32 v14, v15
	v_permlane32_swap_b32_e32 v16, v27
	v_permlane32_swap_b32_e32 v10, v11
	v_permlane32_swap_b32_e32 v3, v13
	v_permlane32_swap_b32_e32 v2, v36
	v_add_f32_e32 v9, v9, v23
	v_add_f32_e32 v24, v24, v25
	v_add_f32_e32 v6, v6, v7
	v_add_f32_e32 v8, v8, v17
	v_add_f32_e32 v18, v18, v19
	v_add_f32_e32 v20, v20, v26
	v_add_f32_e32 v14, v14, v15
	v_add_f32_e32 v16, v16, v27
	v_add_f32_e32 v10, v10, v11
	v_add_f32_e32 v3, v3, v13
	v_add_f32_e32 v2, v2, v36
	s_nop 0
	v_permlane16_swap_b32_e32 v9, v24
	v_permlane16_swap_b32_e32 v6, v8
	v_permlane16_swap_b32_e32 v18, v20
	v_permlane16_swap_b32_e32 v14, v16
	v_permlane16_swap_b32_e32 v10, v3
	v_add_f32_e32 v9, v9, v24
	v_add_f32_e32 v6, v6, v8
	v_add_f32_e32 v18, v18, v20
	v_add_f32_e32 v14, v14, v16
	v_add_f32_e32 v10, v10, v3
	v_add_f32_dpp v9, v9, v9 row_shr:1 row_mask:0xf bank_mask:0xf bound_ctrl:1
	v_add_f32_dpp v6, v6, v6 row_shr:1 row_mask:0xf bank_mask:0xf bound_ctrl:1
	v_add_f32_dpp v18, v18, v18 row_shr:1 row_mask:0xf bank_mask:0xf bound_ctrl:1
	v_add_f32_dpp v14, v14, v14 row_shr:1 row_mask:0xf bank_mask:0xf bound_ctrl:1
	v_add_f32_dpp v10, v10, v10 row_shr:1 row_mask:0xf bank_mask:0xf bound_ctrl:1
	v_add_f32_dpp v2, v2, v2 row_shr:1 row_mask:0xf bank_mask:0xf bound_ctrl:1
	v_add_f32_dpp v9, v9, v9 row_shr:2 row_mask:0xf bank_mask:0xf bound_ctrl:1
	v_add_f32_dpp v6, v6, v6 row_shr:2 row_mask:0xf bank_mask:0xf bound_ctrl:1
	v_add_f32_dpp v18, v18, v18 row_shr:2 row_mask:0xf bank_mask:0xf bound_ctrl:1
	v_add_f32_dpp v14, v14, v14 row_shr:2 row_mask:0xf bank_mask:0xf bound_ctrl:1
	v_add_f32_dpp v10, v10, v10 row_shr:2 row_mask:0xf bank_mask:0xf bound_ctrl:1
	v_add_f32_dpp v2, v2, v2 row_shr:2 row_mask:0xf bank_mask:0xf bound_ctrl:1
	v_add_f32_dpp v9, v9, v9 row_shr:4 row_mask:0xf bank_mask:0xf bound_ctrl:1
	v_add_f32_dpp v6, v6, v6 row_shr:4 row_mask:0xf bank_mask:0xf bound_ctrl:1
	v_add_f32_dpp v18, v18, v18 row_shr:4 row_mask:0xf bank_mask:0xf bound_ctrl:1
	v_add_f32_dpp v14, v14, v14 row_shr:4 row_mask:0xf bank_mask:0xf bound_ctrl:1
	v_add_f32_dpp v10, v10, v10 row_shr:4 row_mask:0xf bank_mask:0xf bound_ctrl:1
	v_add_f32_dpp v2, v2, v2 row_shr:4 row_mask:0xf bank_mask:0xf bound_ctrl:1
	v_add_f32_dpp v9, v9, v9 row_shr:8 row_mask:0xf bank_mask:0xf bound_ctrl:1
	v_add_f32_dpp v6, v6, v6 row_shr:8 row_mask:0xf bank_mask:0xf bound_ctrl:1
	v_add_f32_dpp v18, v18, v18 row_shr:8 row_mask:0xf bank_mask:0xf bound_ctrl:1
	v_add_f32_dpp v14, v14, v14 row_shr:8 row_mask:0xf bank_mask:0xf bound_ctrl:1
	v_add_f32_dpp v10, v10, v10 row_shr:8 row_mask:0xf bank_mask:0xf bound_ctrl:1
	v_add_f32_dpp v2, v2, v2 row_shr:8 row_mask:0xf bank_mask:0xf bound_ctrl:1
	s_nop 1
	v_add_f32_dpp v2, v2, v2 row_bcast:15 row_mask:0xa bank_mask:0xf
	v_and_b32_e32 v37, 15, v46
	v_cmp_eq_u32_e64 s[52:53], 15, v37
	s_and_saveexec_b64 s[6:7], s[52:53]
	s_cbranch_execz .LBB1_30
	v_lshl_or_b32 v4, v4, 4, s28
	s_movk_i32 s4, 0x60
	v_mov_b64_e32 v[28:29], s[22:23]
	v_mad_u64_u32 v[28:29], s[4:5], v4, s4, v[28:29]
	v_lshrrev_b32_e32 v50, 4, v46
	v_lshlrev_b32_e32 v52, 1, v50
	v_bfe_u32 v51, v50, 1, 1
	v_and_b32_e32 v52, 2, v52
	v_or_b32_e32 v52, v52, v51
	v_cmp_gt_u32_e32 vcc, 2, v50
	v_xor_b32_e32 v51, 1, v50
	v_mov_b32_e32 v55, 0
	v_lshlrev_b32_e32 v54, 2, v52
	v_cndmask_b32_e32 v51, v50, v51, vcc
	v_lshl_add_u64 v[56:57], v[28:29], 0, v[54:55]
	v_lshlrev_b32_e32 v54, 2, v51
	v_lshl_add_u64 v[58:59], v[28:29], 0, v[54:55]
	global_store_dword v[56:57], v9, off
	global_store_dword v[56:57], v6, off offset:16
	global_store_dword v[56:57], v18, off offset:32
	global_store_dword v[56:57], v14, off offset:48
	global_store_dword v[56:57], v10, off offset:64
	global_store_dword v[58:59], v2, off offset:80
